# speedup vs baseline: 1.0067x; 1.0027x over previous
_Z7k_protoPKfPf:
	s_and_b32 s11, s2, 7
	s_lshr_b32 s12, s2, 3
	s_mul_i32 s11, s11, 5
	s_add_i32 s2, s11, s12
	s_load_dwordx4 s[4:7], s[0:1], 0x0
	v_and_b32_e32 v1, 15, v0
	v_lshrrev_b32_e32 v46, 4, v0
	s_lshl_b32 s0, s3, 11
	v_lshl_or_b32 v18, v46, 6, s0
	v_lshlrev_b32_e32 v42, 4, v1
	v_mov_b32_e32 v43, 0
	s_waitcnt lgkmcnt(0)
	v_lshl_add_u64 v[20:21], s[4:5], 0, v[42:43]
	v_ashrrev_i32_e32 v19, 31, v18
	s_mul_i32 s8, s2, 5
	v_lshl_add_u64 v[30:31], v[18:19], 2, v[20:21]
	v_mov_b32_e32 v43, 0x28000
	v_or_b32_e32 v18, 0x400, v18
	v_mad_i64_i32 v[10:11], s[0:1], s8, v43, v[30:31]
	s_add_i32 s4, s8, 1
	s_add_i32 s5, s8, 2
	v_ashrrev_i32_e32 v19, 31, v18
	v_mad_i64_i32 v[12:13], s[0:1], s4, v43, v[30:31]
	global_load_dwordx4 v[2:5], v[10:11], off nt
	global_load_dwordx4 v[6:9], v[12:13], off nt
	v_mad_i64_i32 v[22:23], s[0:1], s5, v43, v[30:31]
	s_add_i32 s9, s8, 3
	v_lshl_add_u64 v[38:39], v[18:19], 2, v[20:21]
	v_mad_i64_i32 v[24:25], s[0:1], s9, v43, v[30:31]
	global_load_dwordx4 v[10:13], v[22:23], off nt
	global_load_dwordx4 v[14:17], v[24:25], off nt
	v_mad_i64_i32 v[18:19], s[0:1], s8, v43, v[38:39]
	v_mad_i64_i32 v[22:23], s[0:1], s4, v43, v[38:39]
	s_add_i32 s10, s8, 4
	global_load_dwordx4 v[18:21], v[18:19], off nt
	v_mad_i64_i32 v[26:27], s[0:1], s5, v43, v[38:39]
	global_load_dwordx4 v[22:25], v[22:23], off nt
	v_mad_i64_i32 v[44:45], s[0:1], s9, v43, v[38:39]
	global_load_dwordx4 v[26:29], v[26:27], off nt
	v_mad_i64_i32 v[40:41], s[0:1], s10, v43, v[30:31]
	global_load_dwordx4 v[30:33], v[44:45], off nt
	global_load_dwordx4 v[34:37], v[40:41], off nt
	v_mad_i64_i32 v[38:39], s[0:1], s10, v43, v[38:39]
	global_load_dwordx4 v[38:41], v[38:39], off nt
	s_movk_i32 s1, 0x120
	s_mov_b32 s0, 0x3e4ccccd
	v_lshrrev_b32_e32 v43, 3, v0
	v_bfe_u32 v44, v0, 4, 2
	v_and_or_b32 v43, v43, 24, v44
	v_lshlrev_b32_e32 v43, 1, v43
	v_mad_u32_u24 v43, v1, s1, v43
	v_cmp_gt_u32_e32 vcc, 64, v0
	s_mul_i32 s4, s2, 20
	v_lshl_or_b32 v42, v46, 8, v42
	s_waitcnt vmcnt(8)
	v_pk_add_f32 v[2:3], v[2:3], v[6:7]
	v_pk_add_f32 v[4:5], v[4:5], v[8:9]
	s_waitcnt vmcnt(7)
	v_pk_add_f32 v[2:3], v[2:3], v[10:11]
	s_waitcnt vmcnt(6)
	v_pk_add_f32 v[2:3], v[2:3], v[14:15]
	v_pk_add_f32 v[4:5], v[4:5], v[12:13]
	s_waitcnt vmcnt(4)
	v_pk_add_f32 v[8:9], v[18:19], v[22:23]
	v_pk_add_f32 v[6:7], v[20:21], v[24:25]
	v_pk_add_f32 v[4:5], v[4:5], v[16:17]
	s_waitcnt vmcnt(3)
	v_pk_add_f32 v[8:9], v[8:9], v[26:27]
	v_pk_add_f32 v[6:7], v[6:7], v[28:29]
	s_waitcnt vmcnt(2)
	v_pk_add_f32 v[8:9], v[8:9], v[30:31]
	s_waitcnt vmcnt(1)
	v_pk_add_f32 v[2:3], v[2:3], v[34:35]
	v_pk_add_f32 v[6:7], v[6:7], v[32:33]
	v_pk_mul_f32 v[2:3], v[2:3], s[0:1] op_sel_hi:[1,0]
	s_waitcnt vmcnt(0)
	v_pk_add_f32 v[8:9], v[8:9], v[38:39]
	v_cvt_f16_f32_e32 v10, v2
	v_pk_add_f32 v[4:5], v[4:5], v[36:37]
	v_pk_add_f32 v[6:7], v[6:7], v[40:41]
	v_pk_mul_f32 v[8:9], v[8:9], s[0:1] op_sel_hi:[1,0]
	v_cvt_f16_f32_e32 v11, v3
	v_pk_mul_f32 v[4:5], v[4:5], s[0:1] op_sel_hi:[1,0]
	v_pk_mul_f32 v[6:7], v[6:7], s[0:1] op_sel_hi:[1,0]
	v_cvt_f16_f32_e32 v12, v8
	v_cvt_f16_f32_e32 v13, v9
	v_pk_mul_f32 v[8:9], v[8:9], v[8:9]
	v_cvt_f16_f32_e32 v14, v4
	v_cvt_f16_f32_e32 v16, v6
	v_cvt_f16_f32_e32 v17, v7
	v_pk_mul_f32 v[6:7], v[6:7], v[6:7]
	v_cvt_f16_f32_e32 v15, v5
	v_pk_fma_f32 v[2:3], v[2:3], v[2:3], v[8:9]
	v_pk_fma_f32 v[4:5], v[4:5], v[4:5], v[6:7]
	ds_write_b16 v43, v10
	ds_write_b16 v43, v11 offset:72
	ds_write_b16 v43, v12 offset:8
	ds_write_b16 v43, v14 offset:144
	ds_write_b16 v43, v15 offset:216
	ds_write_b16 v43, v17 offset:224
	ds_write_b16 v43, v13 offset:80
	ds_write_b16 v43, v16 offset:152
	ds_write_b128 v42, v[2:5] offset:4608
	s_waitcnt lgkmcnt(0)
	s_barrier
	s_and_saveexec_b64 s[0:1], vcc
	s_cbranch_execz .LBB0_2
	v_lshlrev_b32_e32 v12, 2, v0
	ds_read2st64_b32 v[2:3], v12 offset0:18 offset1:19
	ds_read2st64_b32 v[4:5], v12 offset0:20 offset1:21
	ds_read2st64_b32 v[6:7], v12 offset0:22 offset1:23
	ds_read2st64_b32 v[8:9], v12 offset0:24 offset1:25
	ds_read2st64_b32 v[10:11], v12 offset0:26 offset1:27
	s_waitcnt lgkmcnt(4)
	v_add_f32_e32 v2, 0, v2
	v_add_f32_e32 v2, v2, v3
	s_waitcnt lgkmcnt(3)
	v_add_f32_e32 v2, v2, v4
	v_add_f32_e32 v2, v2, v5
	s_waitcnt lgkmcnt(2)
	v_add_f32_e32 v2, v2, v6
	v_add_f32_e32 v2, v2, v7
	s_waitcnt lgkmcnt(1)
	v_add_f32_e32 v2, v2, v8
	v_add_f32_e32 v8, v2, v9
	ds_read2st64_b32 v[2:3], v12 offset0:28 offset1:29
	ds_read2st64_b32 v[4:5], v12 offset0:30 offset1:31
	ds_read2st64_b32 v[6:7], v12 offset0:32 offset1:33
	s_waitcnt lgkmcnt(3)
	v_add_f32_e32 v8, v8, v10
	v_add_f32_e32 v8, v8, v11
	s_waitcnt lgkmcnt(2)
	v_add_f32_e32 v2, v8, v2
	v_add_f32_e32 v2, v2, v3
	s_waitcnt lgkmcnt(1)
	v_add_f32_e32 v2, v2, v4
	v_add_f32_e32 v2, v2, v5
	s_waitcnt lgkmcnt(0)
	v_add_f32_e32 v2, v2, v6
	s_add_i32 s5, s4, s3
	v_add_f32_e32 v4, v2, v7
	v_lshl_or_b32 v2, s5, 6, v0
	v_ashrrev_i32_e32 v3, 31, v2
	v_lshl_add_u64 v[2:3], v[2:3], 2, s[6:7]
	global_store_dword v[2:3], v4, off

	.amdhsa_kernel _Z7k_protoPKfPf
		.amdhsa_group_segment_fixed_size 8704
		.amdhsa_private_segment_fixed_size 0
		.amdhsa_kernarg_size 16
		.amdhsa_user_sgpr_count 2
		.amdhsa_user_sgpr_dispatch_ptr 0
		.amdhsa_user_sgpr_queue_ptr 0
		.amdhsa_user_sgpr_kernarg_segment_ptr 1
		.amdhsa_user_sgpr_dispatch_id 0
		.amdhsa_user_sgpr_kernarg_preload_length 0
		.amdhsa_user_sgpr_kernarg_preload_offset 0
		.amdhsa_user_sgpr_private_segment_size 0
		.amdhsa_uses_dynamic_stack 0
		.amdhsa_enable_private_segment 0
		.amdhsa_system_sgpr_workgroup_id_x 1
		.amdhsa_system_sgpr_workgroup_id_y 1
		.amdhsa_system_sgpr_workgroup_id_z 0
		.amdhsa_system_sgpr_workgroup_info 0
		.amdhsa_system_vgpr_workitem_id 0
		.amdhsa_next_free_vgpr 47
		.amdhsa_next_free_sgpr 16
		.amdhsa_accum_offset 48
		.amdhsa_reserve_vcc 1
		.amdhsa_float_round_mode_32 0
		.amdhsa_float_round_mode_16_64 0
		.amdhsa_float_denorm_mode_32 3
		.amdhsa_float_denorm_mode_16_64 3
		.amdhsa_dx10_clamp 1
		.amdhsa_ieee_mode 1
		.amdhsa_fp16_overflow 0
		.amdhsa_tg_split 0
		.amdhsa_exception_fp_ieee_invalid_op 0
		.amdhsa_exception_fp_denorm_src 0
		.amdhsa_exception_fp_ieee_div_zero 0
		.amdhsa_exception_fp_ieee_overflow 0
		.amdhsa_exception_fp_ieee_underflow 0
		.amdhsa_exception_fp_ieee_inexact 0
		.amdhsa_exception_int_div_zero 0
	.end_amdhsa_kernel

amdhsa.kernels:
  - .agpr_count:     0
    .args:
      - .actual_access:  read_only
        .address_space:  global
        .offset:         0
        .size:           8
        .value_kind:     global_buffer
      - .actual_access:  write_only
        .address_space:  global
        .offset:         8
        .size:           8
        .value_kind:     global_buffer
    .group_segment_fixed_size: 8704
    .kernarg_segment_align: 8
    .kernarg_segment_size: 16
    .language:       OpenCL C
    .language_version:
      - 2
      - 0
    .max_flat_workgroup_size: 256
    .name:           _Z7k_protoPKfPf
    .private_segment_fixed_size: 0
    .sgpr_count:     22
    .sgpr_spill_count: 0
    .symbol:         _Z7k_protoPKfPf.kd
    .uniform_work_group_size: 1
    .uses_dynamic_stack: false
    .vgpr_count:     47
    .vgpr_spill_count: 0
    .wavefront_size: 64
  - .agpr_count:     0
    .args:
      - .actual_access:  read_only
        .address_space:  global
        .offset:         0
        .size:           8
        .value_kind:     global_buffer
      - .actual_access:  read_only
        .address_space:  global
        .offset:         8
        .size:           8
        .value_kind:     global_buffer
      - .actual_access:  write_only
        .address_space:  global
        .offset:         16
        .size:           8
        .value_kind:     global_buffer
    .group_segment_fixed_size: 53760
    .kernarg_segment_align: 8
    .kernarg_segment_size: 24
    .language:       OpenCL C
    .language_version:
      - 2
      - 0
    .max_flat_workgroup_size: 320
    .name:           _Z7k_fusedPKfPfS1_
    .private_segment_fixed_size: 0
    .sgpr_count:     34
    .sgpr_spill_count: 0
    .symbol:         _Z7k_fusedPKfPfS1_.kd
    .uniform_work_group_size: 1
    .uses_dynamic_stack: false
    .vgpr_count:     123
    .vgpr_spill_count: 0
    .wavefront_size: 64
